# baseline (speedup 1.0000x reference)
.LBB1_8:
	s_or_b64 exec, exec, s[2:3]
	v_bfe_u32 v18, v0, 4, 1
	v_lshl_or_b32 v18, v163, 1, v18
	v_and_b32_e32 v22, 15, v0
	v_mad_u32_u24 v18, v18, 18, v22
	s_movk_i32 s2, 0x50
	v_mad_u32_u24 v23, v18, s2, v162
	s_waitcnt lgkmcnt(0)
	s_barrier
	s_cmp_lt_u32 s38, 0x100
	s_cbranch_scc1 .Lk2_nostag
	s_sleep 4
.Lk2_nostag:
	ds_read_b128 v[18:21], v23 offset:32000
	ds_read_b128 v[24:27], v23 offset:32032
	ds_read_b128 v[28:31], v23 offset:32080
	ds_read_b128 v[32:35], v23 offset:32112
	ds_read_b128 v[36:39], v23 offset:32160
	ds_read_b128 v[40:43], v23 offset:32192
	ds_read_b128 v[44:47], v23 offset:33440
	ds_read_b128 v[166:169], v23 offset:33472
	ds_read_b128 v[170:173], v23 offset:33520
	s_waitcnt vmcnt(12) lgkmcnt(8)
	v_mfma_f32_32x32x16_f16 v[2:17], v[150:153], v[18:21], v[2:17]
	s_waitcnt lgkmcnt(7)
	v_mfma_f32_32x32x16_f16 v[2:17], v[146:149], v[24:27], v[2:17]
	ds_read_b128 v[18:21], v23 offset:33552
	s_waitcnt lgkmcnt(7)
	v_mfma_f32_32x32x16_f16 v[2:17], v[142:145], v[28:31], v[2:17]
	ds_read_b128 v[24:27], v23 offset:33600
	s_waitcnt lgkmcnt(7)
	v_mfma_f32_32x32x16_f16 v[2:17], v[138:141], v[32:35], v[2:17]
	ds_read_b128 v[28:31], v23 offset:33632
	s_waitcnt lgkmcnt(7)
	v_mfma_f32_32x32x16_f16 v[2:17], v[134:137], v[36:39], v[2:17]
	ds_read_b128 v[32:35], v23 offset:34880
	s_waitcnt lgkmcnt(7)
	v_mfma_f32_32x32x16_f16 v[2:17], v[130:133], v[40:43], v[2:17]
	ds_read_b128 v[36:39], v23 offset:34912
	s_waitcnt lgkmcnt(7)
	v_mfma_f32_32x32x16_f16 v[2:17], v[126:129], v[44:47], v[2:17]
	ds_read_b128 v[40:43], v23 offset:34960
	s_waitcnt lgkmcnt(7)
	v_mfma_f32_32x32x16_f16 v[2:17], v[122:125], v[166:169], v[2:17]
	ds_read_b128 v[44:47], v23 offset:34992
	s_waitcnt lgkmcnt(7)
	v_mfma_f32_32x32x16_f16 v[2:17], v[118:121], v[170:173], v[2:17]
	ds_read_b128 v[122:125], v23 offset:35040
	s_waitcnt lgkmcnt(7)
	v_mfma_f32_32x32x16_f16 v[2:17], v[114:117], v[18:21], v[2:17]
	ds_read_b128 v[118:121], v23 offset:35072
	s_waitcnt lgkmcnt(7)
	v_mfma_f32_32x32x16_f16 v[2:17], v[110:113], v[24:27], v[2:17]
	s_waitcnt lgkmcnt(6)
	v_mfma_f32_32x32x16_f16 v[2:17], v[106:109], v[28:31], v[2:17]
	s_waitcnt lgkmcnt(5)
	v_mfma_f32_32x32x16_f16 v[2:17], v[102:105], v[32:35], v[2:17]
	s_waitcnt lgkmcnt(4)
	v_mfma_f32_32x32x16_f16 v[2:17], v[98:101], v[36:39], v[2:17]
	s_waitcnt lgkmcnt(3)
	v_mfma_f32_32x32x16_f16 v[2:17], v[94:97], v[40:43], v[2:17]
	s_waitcnt lgkmcnt(2)
	v_mfma_f32_32x32x16_f16 v[2:17], v[90:93], v[44:47], v[2:17]
	s_waitcnt lgkmcnt(1)
	v_mfma_f32_32x32x16_f16 v[2:17], v[86:89], v[122:125], v[2:17]
	s_waitcnt lgkmcnt(0)
	v_mfma_f32_32x32x16_f16 v[2:17], v[82:85], v[118:121], v[2:17]
	s_nop 11
	v_max_f32_dpp v2, v2, v2 quad_perm:[1,0,3,2] row_mask:0xf bank_mask:0xf
	v_max_f32_dpp v3, v3, v3 quad_perm:[1,0,3,2] row_mask:0xf bank_mask:0xf
	v_max_f32_dpp v4, v4, v4 quad_perm:[1,0,3,2] row_mask:0xf bank_mask:0xf
	v_max_f32_dpp v5, v5, v5 quad_perm:[1,0,3,2] row_mask:0xf bank_mask:0xf
	v_max_f32_dpp v6, v6, v6 quad_perm:[1,0,3,2] row_mask:0xf bank_mask:0xf
	v_max_f32_dpp v7, v7, v7 quad_perm:[1,0,3,2] row_mask:0xf bank_mask:0xf
	v_max_f32_dpp v8, v8, v8 quad_perm:[1,0,3,2] row_mask:0xf bank_mask:0xf
	v_max_f32_dpp v9, v9, v9 quad_perm:[1,0,3,2] row_mask:0xf bank_mask:0xf
	v_max_f32_dpp v10, v10, v10 quad_perm:[1,0,3,2] row_mask:0xf bank_mask:0xf
	v_max_f32_dpp v11, v11, v11 quad_perm:[1,0,3,2] row_mask:0xf bank_mask:0xf
	v_max_f32_dpp v12, v12, v12 quad_perm:[1,0,3,2] row_mask:0xf bank_mask:0xf
	v_max_f32_dpp v13, v13, v13 quad_perm:[1,0,3,2] row_mask:0xf bank_mask:0xf
	v_max_f32_dpp v14, v14, v14 quad_perm:[1,0,3,2] row_mask:0xf bank_mask:0xf
	v_max_f32_dpp v15, v15, v15 quad_perm:[1,0,3,2] row_mask:0xf bank_mask:0xf
	v_max_f32_dpp v16, v16, v16 quad_perm:[1,0,3,2] row_mask:0xf bank_mask:0xf
	v_max_f32_dpp v17, v17, v17 quad_perm:[1,0,3,2] row_mask:0xf bank_mask:0xf
	v_permlane16_swap_b32 v2, v4
	v_permlane16_swap_b32 v3, v5
	v_permlane16_swap_b32 v6, v8
	v_permlane16_swap_b32 v7, v9
	v_permlane16_swap_b32 v10, v12
	v_permlane16_swap_b32 v11, v13
	v_permlane16_swap_b32 v14, v16
	v_permlane16_swap_b32 v15, v17
	v_and_b32_e32 v18, 1, v0
	v_cmp_eq_u32_e32 vcc, 1, v18
	v_max3_f32 v2, v2, v4, 0
	v_max3_f32 v3, v3, v5, 0
	v_max3_f32 v6, v6, v8, 0
	v_max3_f32 v7, v7, v9, 0
	v_max3_f32 v10, v10, v12, 0
	v_max3_f32 v11, v11, v13, 0
	v_max3_f32 v14, v14, v16, 0
	v_max3_f32 v15, v15, v17, 0
	v_cndmask_b32_e32 v20, v2, v3, vcc
	v_cndmask_b32_e32 v22, v6, v7, vcc
	v_cndmask_b32_e32 v24, v10, v11, vcc
	v_cndmask_b32_e32 v26, v14, v15, vcc
	s_waitcnt vmcnt(0)
	v_pk_fma_f32 v[2:3], v[20:21], v[66:67], 0 op_sel_hi:[0,1,0]
	v_pk_fma_f32 v[6:7], v[20:21], v[68:69], 0 op_sel_hi:[0,1,0]
	v_pk_fma_f32 v[10:11], v[20:21], v[50:51], 0 op_sel_hi:[0,1,0]
	v_pk_fma_f32 v[14:15], v[20:21], v[52:53], 0 op_sel_hi:[0,1,0]
	v_pk_fma_f32 v[18:19], v[20:21], v[156:157], 0 op_sel_hi:[0,1,0]
	v_pk_fma_f32 v[2:3], v[22:23], v[70:71], v[2:3] op_sel_hi:[0,1,1]
	v_pk_fma_f32 v[6:7], v[22:23], v[72:73], v[6:7] op_sel_hi:[0,1,1]
	v_pk_fma_f32 v[10:11], v[22:23], v[54:55], v[10:11] op_sel_hi:[0,1,1]
	v_pk_fma_f32 v[14:15], v[22:23], v[56:57], v[14:15] op_sel_hi:[0,1,1]
	v_pk_fma_f32 v[18:19], v[22:23], v[154:155], v[18:19] op_sel_hi:[0,1,1]
	v_pk_fma_f32 v[2:3], v[24:25], v[74:75], v[2:3] op_sel_hi:[0,1,1]
	v_pk_fma_f32 v[6:7], v[24:25], v[76:77], v[6:7] op_sel_hi:[0,1,1]
	v_pk_fma_f32 v[10:11], v[24:25], v[58:59], v[10:11] op_sel_hi:[0,1,1]
	v_pk_fma_f32 v[14:15], v[24:25], v[60:61], v[14:15] op_sel_hi:[0,1,1]
	v_pk_fma_f32 v[18:19], v[24:25], v[160:161], v[18:19] op_sel_hi:[0,1,1]
	v_pk_fma_f32 v[2:3], v[26:27], v[78:79], v[2:3] op_sel_hi:[0,1,1]
	v_pk_fma_f32 v[6:7], v[26:27], v[80:81], v[6:7] op_sel_hi:[0,1,1]
	v_pk_fma_f32 v[10:11], v[26:27], v[62:63], v[10:11] op_sel_hi:[0,1,1]
	v_pk_fma_f32 v[14:15], v[26:27], v[64:65], v[14:15] op_sel_hi:[0,1,1]
	v_pk_fma_f32 v[18:19], v[26:27], v[158:159], v[18:19] op_sel_hi:[0,1,1]
	v_and_b32_e32 v28, 15, v0
	v_cmp_eq_u32_e32 vcc, 15, v28
	v_add_f32_dpp v2, v2, v2 row_shr:1 row_mask:0xf bank_mask:0xf bound_ctrl:1
	v_add_f32_dpp v3, v3, v3 row_shr:1 row_mask:0xf bank_mask:0xf bound_ctrl:1
	v_add_f32_dpp v6, v6, v6 row_shr:1 row_mask:0xf bank_mask:0xf bound_ctrl:1
	v_add_f32_dpp v7, v7, v7 row_shr:1 row_mask:0xf bank_mask:0xf bound_ctrl:1
	v_add_f32_dpp v10, v10, v10 row_shr:1 row_mask:0xf bank_mask:0xf bound_ctrl:1
	v_add_f32_dpp v11, v11, v11 row_shr:1 row_mask:0xf bank_mask:0xf bound_ctrl:1
	v_add_f32_dpp v14, v14, v14 row_shr:1 row_mask:0xf bank_mask:0xf bound_ctrl:1
	v_add_f32_dpp v15, v15, v15 row_shr:1 row_mask:0xf bank_mask:0xf bound_ctrl:1
	v_add_f32_dpp v18, v18, v18 row_shr:1 row_mask:0xf bank_mask:0xf bound_ctrl:1
	v_add_f32_dpp v19, v19, v19 row_shr:1 row_mask:0xf bank_mask:0xf bound_ctrl:1
	v_add_f32_dpp v2, v2, v2 row_shr:2 row_mask:0xf bank_mask:0xf bound_ctrl:1
	v_add_f32_dpp v3, v3, v3 row_shr:2 row_mask:0xf bank_mask:0xf bound_ctrl:1
	v_add_f32_dpp v6, v6, v6 row_shr:2 row_mask:0xf bank_mask:0xf bound_ctrl:1
	v_add_f32_dpp v7, v7, v7 row_shr:2 row_mask:0xf bank_mask:0xf bound_ctrl:1
	v_add_f32_dpp v10, v10, v10 row_shr:2 row_mask:0xf bank_mask:0xf bound_ctrl:1
	v_add_f32_dpp v11, v11, v11 row_shr:2 row_mask:0xf bank_mask:0xf bound_ctrl:1
	v_add_f32_dpp v14, v14, v14 row_shr:2 row_mask:0xf bank_mask:0xf bound_ctrl:1
	v_add_f32_dpp v15, v15, v15 row_shr:2 row_mask:0xf bank_mask:0xf bound_ctrl:1
	v_add_f32_dpp v18, v18, v18 row_shr:2 row_mask:0xf bank_mask:0xf bound_ctrl:1
	v_add_f32_dpp v19, v19, v19 row_shr:2 row_mask:0xf bank_mask:0xf bound_ctrl:1
	v_add_f32_dpp v2, v2, v2 row_shr:4 row_mask:0xf bank_mask:0xf bound_ctrl:1
	v_add_f32_dpp v3, v3, v3 row_shr:4 row_mask:0xf bank_mask:0xf bound_ctrl:1
	v_add_f32_dpp v6, v6, v6 row_shr:4 row_mask:0xf bank_mask:0xf bound_ctrl:1
	v_add_f32_dpp v7, v7, v7 row_shr:4 row_mask:0xf bank_mask:0xf bound_ctrl:1
	v_add_f32_dpp v10, v10, v10 row_shr:4 row_mask:0xf bank_mask:0xf bound_ctrl:1
	v_add_f32_dpp v11, v11, v11 row_shr:4 row_mask:0xf bank_mask:0xf bound_ctrl:1
	v_add_f32_dpp v14, v14, v14 row_shr:4 row_mask:0xf bank_mask:0xf bound_ctrl:1
	v_add_f32_dpp v15, v15, v15 row_shr:4 row_mask:0xf bank_mask:0xf bound_ctrl:1
	v_add_f32_dpp v18, v18, v18 row_shr:4 row_mask:0xf bank_mask:0xf bound_ctrl:1
	v_add_f32_dpp v19, v19, v19 row_shr:4 row_mask:0xf bank_mask:0xf bound_ctrl:1
	v_add_f32_dpp v2, v2, v2 row_shr:8 row_mask:0xf bank_mask:0xf bound_ctrl:1
	v_add_f32_dpp v3, v3, v3 row_shr:8 row_mask:0xf bank_mask:0xf bound_ctrl:1
	v_add_f32_dpp v6, v6, v6 row_shr:8 row_mask:0xf bank_mask:0xf bound_ctrl:1
	v_add_f32_dpp v7, v7, v7 row_shr:8 row_mask:0xf bank_mask:0xf bound_ctrl:1
	v_add_f32_dpp v10, v10, v10 row_shr:8 row_mask:0xf bank_mask:0xf bound_ctrl:1
	v_add_f32_dpp v11, v11, v11 row_shr:8 row_mask:0xf bank_mask:0xf bound_ctrl:1
	v_add_f32_dpp v14, v14, v14 row_shr:8 row_mask:0xf bank_mask:0xf bound_ctrl:1
	v_add_f32_dpp v15, v15, v15 row_shr:8 row_mask:0xf bank_mask:0xf bound_ctrl:1
	v_add_f32_dpp v18, v18, v18 row_shr:8 row_mask:0xf bank_mask:0xf bound_ctrl:1
	v_add_f32_dpp v19, v19, v19 row_shr:8 row_mask:0xf bank_mask:0xf bound_ctrl:1
	s_and_saveexec_b64 s[2:3], vcc
	s_cbranch_execz .LBB1_12
	v_lshrrev_b32_e32 v1, 4, v1
	v_mul_u32_u24_e32 v22, 0xa0, v163
	v_mul_u32_u24_e32 v1, 40, v1
	s_mov_b32 s4, 0x14a40
	v_add3_u32 v1, v22, v1, s4
	ds_write2_b64 v1, v[2:3], v[6:7] offset1:1
	ds_write2_b64 v1, v[10:11], v[14:15] offset0:2 offset1:3
	ds_write_b64 v1, v[18:19] offset:32
